# baseline (speedup 1.0000x reference)
_Z13logits_kernelPKDv8_DF16bS1_PKfS3_PDv2_fS5_Pf:
	s_load_dwordx4 s[4:7], s[0:1], 0x0
	s_load_dwordx4 s[12:15], s[0:1], 0x10
	s_load_dwordx4 s[24:27], s[0:1], 0x20
	s_load_dwordx2 s[28:29], s[0:1], 0x30
	s_lshl_b32 s3, s2, 1
	s_and_b32 s3, s3, 14
	s_ashr_i32 s8, s2, 7
	s_bfe_u32 s10, s2, 0x40003
	s_add_i32 s3, s3, s8
	v_lshrrev_b32_e32 v1, 6, v0
	v_and_b32_e32 v2, 63, v0
	s_movk_i32 s11, 0x3000
	v_lshlrev_b32_e32 v2, 4, v2
	v_and_b32_e32 v5, 31, v0
	v_mad_u32_u24 v2, v1, s11, v2
	v_lshlrev_b32_e32 v5, 2, v5
	s_lshl_b32 s9, s3, 9
	v_add_u32_e32 v3, 0x1000, v2
	v_add_u32_e32 v4, 0x2000, v2
	v_add_u32_e32 v5, s9, v5
	s_mul_i32 s8, s10, 0xc000
	s_mul_i32 s9, s3, 0x30000
	s_waitcnt lgkmcnt(0)
	s_load_dword s22, s[14:15], 0x0
	global_load_dword v248, v5, s[12:13]
	global_load_dword v249, v5, s[12:13] offset:128
	global_load_dword v250, v5, s[12:13] offset:256
	global_load_dword v251, v5, s[12:13] offset:384
	s_add_u32 s4, s4, s8
	s_addc_u32 s5, s5, 0
	s_add_u32 s6, s6, s9
	s_addc_u32 s7, s7, 0
	s_add_u32 s16, s6, 0xc000
	s_addc_u32 s17, s7, 0
	s_add_u32 s18, s6, 0x18000
	s_addc_u32 s19, s7, 0
	s_add_u32 s20, s6, 0x24000
	s_addc_u32 s21, s7, 0
	global_load_dwordx4 v[8:11], v2, s[4:5] nt
	global_load_dwordx4 v[56:59], v2, s[6:7]
	global_load_dwordx4 v[104:107], v2, s[16:17]
	global_load_dwordx4 v[152:155], v2, s[18:19]
	global_load_dwordx4 v[200:203], v2, s[20:21]
	global_load_dwordx4 v[12:15], v2, s[4:5] offset:1024 nt
	global_load_dwordx4 v[60:63], v2, s[6:7] offset:1024
	global_load_dwordx4 v[108:111], v2, s[16:17] offset:1024
	global_load_dwordx4 v[156:159], v2, s[18:19] offset:1024
	global_load_dwordx4 v[204:207], v2, s[20:21] offset:1024
	global_load_dwordx4 v[16:19], v2, s[4:5] offset:2048 nt
	global_load_dwordx4 v[64:67], v2, s[6:7] offset:2048
	global_load_dwordx4 v[112:115], v2, s[16:17] offset:2048
	global_load_dwordx4 v[160:163], v2, s[18:19] offset:2048
	global_load_dwordx4 v[208:211], v2, s[20:21] offset:2048
	global_load_dwordx4 v[20:23], v2, s[4:5] offset:3072 nt
	global_load_dwordx4 v[68:71], v2, s[6:7] offset:3072
	global_load_dwordx4 v[116:119], v2, s[16:17] offset:3072
	global_load_dwordx4 v[164:167], v2, s[18:19] offset:3072
	global_load_dwordx4 v[212:215], v2, s[20:21] offset:3072
	global_load_dwordx4 v[24:27], v3, s[4:5] nt
	global_load_dwordx4 v[72:75], v3, s[6:7]
	global_load_dwordx4 v[120:123], v3, s[16:17]
	global_load_dwordx4 v[168:171], v3, s[18:19]
	global_load_dwordx4 v[216:219], v3, s[20:21]
	global_load_dwordx4 v[28:31], v3, s[4:5] offset:1024 nt
	global_load_dwordx4 v[76:79], v3, s[6:7] offset:1024
	global_load_dwordx4 v[124:127], v3, s[16:17] offset:1024
	global_load_dwordx4 v[172:175], v3, s[18:19] offset:1024
	global_load_dwordx4 v[220:223], v3, s[20:21] offset:1024
	global_load_dwordx4 v[32:35], v3, s[4:5] offset:2048 nt
	global_load_dwordx4 v[80:83], v3, s[6:7] offset:2048
	global_load_dwordx4 v[128:131], v3, s[16:17] offset:2048
	global_load_dwordx4 v[176:179], v3, s[18:19] offset:2048
	global_load_dwordx4 v[224:227], v3, s[20:21] offset:2048
	global_load_dwordx4 v[36:39], v3, s[4:5] offset:3072 nt
	global_load_dwordx4 v[84:87], v3, s[6:7] offset:3072
	global_load_dwordx4 v[132:135], v3, s[16:17] offset:3072
	global_load_dwordx4 v[180:183], v3, s[18:19] offset:3072
	global_load_dwordx4 v[228:231], v3, s[20:21] offset:3072
	global_load_dwordx4 v[40:43], v4, s[4:5] nt
	global_load_dwordx4 v[88:91], v4, s[6:7]
	global_load_dwordx4 v[136:139], v4, s[16:17]
	global_load_dwordx4 v[184:187], v4, s[18:19]
	global_load_dwordx4 v[232:235], v4, s[20:21]
	global_load_dwordx4 v[44:47], v4, s[4:5] offset:1024 nt
	global_load_dwordx4 v[92:95], v4, s[6:7] offset:1024
	global_load_dwordx4 v[140:143], v4, s[16:17] offset:1024
	global_load_dwordx4 v[188:191], v4, s[18:19] offset:1024
	global_load_dwordx4 v[236:239], v4, s[20:21] offset:1024
	global_load_dwordx4 v[48:51], v4, s[4:5] offset:2048 nt
	global_load_dwordx4 v[96:99], v4, s[6:7] offset:2048
	global_load_dwordx4 v[144:147], v4, s[16:17] offset:2048
	global_load_dwordx4 v[192:195], v4, s[18:19] offset:2048
	global_load_dwordx4 v[240:243], v4, s[20:21] offset:2048
	global_load_dwordx4 v[52:55], v4, s[4:5] offset:3072 nt
	global_load_dwordx4 v[100:103], v4, s[6:7] offset:3072
	global_load_dwordx4 v[148:151], v4, s[16:17] offset:3072
	global_load_dwordx4 v[196:199], v4, s[18:19] offset:3072
	global_load_dwordx4 v[244:247], v4, s[20:21] offset:3072
	s_waitcnt vmcnt(58)
	v_mfma_f32_32x32x16_bf16 a[0:15], v[8:11], v[56:59], 0
	s_waitcnt vmcnt(57)
	v_mfma_f32_32x32x16_bf16 a[0:15], v[8:11], v[104:107], a[0:15]
	s_waitcnt vmcnt(56)
	v_mfma_f32_32x32x16_bf16 a[0:15], v[8:11], v[152:155], a[0:15]
	s_waitcnt vmcnt(55)
	v_mfma_f32_32x32x16_bf16 a[0:15], v[8:11], v[200:203], a[0:15]
	s_waitcnt vmcnt(53)
	v_mfma_f32_32x32x16_bf16 a[0:15], v[12:15], v[60:63], a[0:15]
	s_waitcnt vmcnt(52)
	v_mfma_f32_32x32x16_bf16 a[0:15], v[12:15], v[108:111], a[0:15]
	s_waitcnt vmcnt(51)
	v_mfma_f32_32x32x16_bf16 a[0:15], v[12:15], v[156:159], a[0:15]
	s_waitcnt vmcnt(50)
	v_mfma_f32_32x32x16_bf16 a[0:15], v[12:15], v[204:207], a[0:15]
	v_add_f32_e32 v8, 0, v248
	v_add_f32_e32 v8, v8, v249
	v_add_f32_e32 v8, v8, v250
	v_add_f32_e32 v8, v8, v251
	v_mov_b32_e32 v9, 0x3fb8aa3b
	s_waitcnt lgkmcnt(0)
	v_mul_f32_e32 v9, s22, v9
	v_exp_f32_e32 v9, v9
	v_add_f32_e32 v10, 0x2b8cbccc, v8
	v_div_scale_f32 v11, s[8:9], v10, v10, v9
	v_rcp_f32_e32 v12, v11
	v_div_scale_f32 v13, vcc, v9, v10, v9
	v_fma_f32 v14, -v11, v12, 1.0
	v_fmac_f32_e32 v12, v14, v12
	v_mul_f32_e32 v14, v13, v12
	v_fma_f32 v15, -v11, v14, v13
	v_fmac_f32_e32 v14, v15, v12
	v_fma_f32 v11, -v11, v14, v13
	v_div_fmas_f32 v11, v11, v12, v14
	v_div_fixup_f32 v9, v11, v10, v9
	v_lshlrev_b32_e32 v10, 2, v0
	v_add_u32_e32 v10, 0x4000, v10
	v_cmp_gt_u32_e32 vcc, 32, v0
	s_and_saveexec_b64 s[8:9], vcc
	ds_write2_b32 v10, v8, v9 offset0:128 offset1:160
	s_mov_b64 exec, s[8:9]
	s_waitcnt vmcnt(48)
	v_mfma_f32_32x32x16_bf16 a[0:15], v[16:19], v[64:67], a[0:15]
	s_waitcnt vmcnt(47)
	v_mfma_f32_32x32x16_bf16 a[0:15], v[16:19], v[112:115], a[0:15]
	s_waitcnt vmcnt(46)
	v_mfma_f32_32x32x16_bf16 a[0:15], v[16:19], v[160:163], a[0:15]
	s_waitcnt vmcnt(45)
	v_mfma_f32_32x32x16_bf16 a[0:15], v[16:19], v[208:211], a[0:15]
	s_waitcnt vmcnt(43)
	v_mfma_f32_32x32x16_bf16 a[0:15], v[20:23], v[68:71], a[0:15]
	s_waitcnt vmcnt(42)
	v_mfma_f32_32x32x16_bf16 a[0:15], v[20:23], v[116:119], a[0:15]
	s_waitcnt vmcnt(41)
	v_mfma_f32_32x32x16_bf16 a[0:15], v[20:23], v[164:167], a[0:15]
	s_waitcnt vmcnt(40)
	v_mfma_f32_32x32x16_bf16 a[0:15], v[20:23], v[212:215], a[0:15]
	s_waitcnt vmcnt(38)
	v_mfma_f32_32x32x16_bf16 a[0:15], v[24:27], v[72:75], a[0:15]
	s_waitcnt vmcnt(37)
	v_mfma_f32_32x32x16_bf16 a[0:15], v[24:27], v[120:123], a[0:15]
	s_waitcnt vmcnt(36)
	v_mfma_f32_32x32x16_bf16 a[0:15], v[24:27], v[168:171], a[0:15]
	s_waitcnt vmcnt(35)
	v_mfma_f32_32x32x16_bf16 a[0:15], v[24:27], v[216:219], a[0:15]
	s_waitcnt vmcnt(33)
	v_mfma_f32_32x32x16_bf16 a[0:15], v[28:31], v[76:79], a[0:15]
	s_waitcnt vmcnt(32)
	v_mfma_f32_32x32x16_bf16 a[0:15], v[28:31], v[124:127], a[0:15]
	s_waitcnt vmcnt(31)
	v_mfma_f32_32x32x16_bf16 a[0:15], v[28:31], v[172:175], a[0:15]
	s_waitcnt vmcnt(30)
	v_mfma_f32_32x32x16_bf16 a[0:15], v[28:31], v[220:223], a[0:15]
	s_waitcnt vmcnt(28)
	v_mfma_f32_32x32x16_bf16 a[0:15], v[32:35], v[80:83], a[0:15]
	s_waitcnt vmcnt(27)
	v_mfma_f32_32x32x16_bf16 a[0:15], v[32:35], v[128:131], a[0:15]
	s_waitcnt vmcnt(26)
	v_mfma_f32_32x32x16_bf16 a[0:15], v[32:35], v[176:179], a[0:15]
	s_waitcnt vmcnt(25)
	v_mfma_f32_32x32x16_bf16 a[0:15], v[32:35], v[224:227], a[0:15]
	s_waitcnt vmcnt(23)
	v_mfma_f32_32x32x16_bf16 a[0:15], v[36:39], v[84:87], a[0:15]
	s_waitcnt vmcnt(22)
	v_mfma_f32_32x32x16_bf16 a[0:15], v[36:39], v[132:135], a[0:15]
	s_waitcnt vmcnt(21)
	v_mfma_f32_32x32x16_bf16 a[0:15], v[36:39], v[180:183], a[0:15]
	s_waitcnt vmcnt(20)
	v_mfma_f32_32x32x16_bf16 a[0:15], v[36:39], v[228:231], a[0:15]
	s_waitcnt vmcnt(18)
	v_mfma_f32_32x32x16_bf16 a[0:15], v[40:43], v[88:91], a[0:15]
	s_waitcnt vmcnt(17)
	v_mfma_f32_32x32x16_bf16 a[0:15], v[40:43], v[136:139], a[0:15]
	s_waitcnt vmcnt(16)
	v_mfma_f32_32x32x16_bf16 a[0:15], v[40:43], v[184:187], a[0:15]
	s_waitcnt vmcnt(15)
	v_mfma_f32_32x32x16_bf16 a[0:15], v[40:43], v[232:235], a[0:15]
	s_waitcnt vmcnt(13)
	v_mfma_f32_32x32x16_bf16 a[0:15], v[44:47], v[92:95], a[0:15]
	s_waitcnt vmcnt(12)
	v_mfma_f32_32x32x16_bf16 a[0:15], v[44:47], v[140:143], a[0:15]
	s_waitcnt vmcnt(11)
	v_mfma_f32_32x32x16_bf16 a[0:15], v[44:47], v[188:191], a[0:15]
	s_waitcnt vmcnt(10)
	v_mfma_f32_32x32x16_bf16 a[0:15], v[44:47], v[236:239], a[0:15]
	s_waitcnt vmcnt(8)
	v_mfma_f32_32x32x16_bf16 a[0:15], v[48:51], v[96:99], a[0:15]
	s_waitcnt vmcnt(7)
	v_mfma_f32_32x32x16_bf16 a[0:15], v[48:51], v[144:147], a[0:15]
	s_waitcnt vmcnt(6)
	v_mfma_f32_32x32x16_bf16 a[0:15], v[48:51], v[192:195], a[0:15]
	s_waitcnt vmcnt(5)
	v_mfma_f32_32x32x16_bf16 a[0:15], v[48:51], v[240:243], a[0:15]
	v_mul_u32_u24_e32 v1, 0x1080, v1
	s_movk_i32 s4, 0x7f
	s_movk_i32 s6, 0x84
	v_cmp_lt_u32_e32 vcc, s4, v0
	v_lshrrev_b32_e32 v11, 3, v0
	v_and_b32_e32 v10, 31, v0
	v_and_b32_e32 v11, 4, v11
	v_mul_u32_u24_e32 v11, 0x84, v11
	v_lshlrev_b32_e32 v9, 2, v10
	v_bfe_u32 v6, v0, 2, 5
	v_and_b32_e32 v7, 3, v0
	v_add3_u32 v1, v1, v11, v9
	v_lshlrev_b32_e32 v8, 3, v7
	s_waitcnt vmcnt(3)
	v_mfma_f32_32x32x16_bf16 a[0:15], v[52:55], v[100:103], a[0:15]
	s_waitcnt vmcnt(2)
	v_mfma_f32_32x32x16_bf16 a[0:15], v[52:55], v[148:151], a[0:15]
	s_waitcnt vmcnt(1)
	v_mfma_f32_32x32x16_bf16 a[0:15], v[52:55], v[196:199], a[0:15]
	s_waitcnt vmcnt(0)
	v_mfma_f32_32x32x16_bf16 a[0:15], v[52:55], v[244:247], a[0:15]
	s_nop 11
	ds_write_b32 v1, a0
	ds_write_b32 v1, a1 offset:132
	ds_write_b32 v1, a2 offset:264
	ds_write_b32 v1, a3 offset:396
	ds_write_b32 v1, a4 offset:1056
	ds_write_b32 v1, a5 offset:1188
	ds_write_b32 v1, a6 offset:1320
	ds_write_b32 v1, a7 offset:1452
	ds_write_b32 v1, a8 offset:2112
	ds_write_b32 v1, a9 offset:2244
	ds_write_b32 v1, a10 offset:2376
	ds_write_b32 v1, a11 offset:2508
	ds_write_b32 v1, a12 offset:3168
	ds_write_b32 v1, a13 offset:3300
	ds_write_b32 v1, a14 offset:3432
	ds_write_b32 v1, a15 offset:3564
	v_bfe_u32 v6, v0, 2, 5
	v_and_b32_e32 v7, 3, v0
	v_lshlrev_b32_e32 v9, 3, v7
	v_readfirstlane_b32 s30, v0
	v_sub_u32_e32 v10, v6, v9
	s_waitcnt lgkmcnt(0)
	s_barrier
	s_cmpk_ge_u32 s30, 0x80
	s_cbranch_scc1 .Llg_k1
	v_mul_u32_u24_e32 v2, 0x84, v6
	v_lshlrev_b32_e32 v8, 5, v7
	v_add_u32_e32 v2, v2, v8
	v_add_u32_e32 v8, 0x4280, v8
	v_add_u32_e32 v3, 0x1080, v2
	v_add_u32_e32 v4, 0x2100, v2
	v_add_u32_e32 v5, 0x3180, v2
	ds_read_b128 v[48:51], v8
	ds_read_b128 v[52:55], v8 offset:16
	ds_read2_b32 v[16:17], v2 offset0:0 offset1:1
	ds_read2_b32 v[18:19], v2 offset0:2 offset1:3
	ds_read2_b32 v[20:21], v2 offset0:4 offset1:5
	ds_read2_b32 v[22:23], v2 offset0:6 offset1:7
	ds_read2_b32 v[24:25], v3 offset0:0 offset1:1
	ds_read2_b32 v[26:27], v3 offset0:2 offset1:3
	ds_read2_b32 v[28:29], v3 offset0:4 offset1:5
	ds_read2_b32 v[30:31], v3 offset0:6 offset1:7
	ds_read2_b32 v[32:33], v4 offset0:0 offset1:1
	ds_read2_b32 v[34:35], v4 offset0:2 offset1:3
	ds_read2_b32 v[36:37], v4 offset0:4 offset1:5
	ds_read2_b32 v[38:39], v4 offset0:6 offset1:7
	s_waitcnt lgkmcnt(4)
	ds_read2_b32 v[40:41], v5 offset0:0 offset1:1
	ds_read2_b32 v[42:43], v5 offset0:2 offset1:3
	ds_read2_b32 v[44:45], v5 offset0:4 offset1:5
	ds_read2_b32 v[46:47], v5 offset0:6 offset1:7
	s_waitcnt lgkmcnt(0)
	s_branch .Llg_join
